# grid barrier: non-leader workgroups poll the cross-XCD release word directly instead of the per-XCD relay word (one hop less per barrier, 18 barriers); same generation compare, own acquire kept
# baseline (speedup 1.0000x reference)
.LBB0_447:
	s_or_b64 exec, exec, s[12:13]
	v_cvt_f32_u32_e32 v5, v3
	s_waitcnt vmcnt(0)
	v_readfirstlane_b32 s0, v4
	v_sub_u32_e32 v4, 0, v3
	v_rcp_iflag_f32_e32 v5, v5
	v_add_u32_e32 v6, s0, v2
	v_mul_f32_e32 v5, 0x4f7ffffe, v5
	v_cvt_u32_f32_e32 v5, v5
	v_mul_lo_u32 v2, v4, v5
	v_mul_hi_u32 v2, v5, v2
	v_add_u32_e32 v2, v5, v2
	v_mul_hi_u32 v2, v6, v2
	v_mul_lo_u32 v4, v2, v3
	v_sub_u32_e32 v4, v6, v4
	v_add_u32_e32 v5, 1, v2
	v_cmp_ge_u32_e32 vcc, v4, v3
	s_nop 1
	v_cndmask_b32_e32 v2, v2, v5, vcc
	v_sub_u32_e32 v5, v4, v3
	v_cndmask_b32_e32 v4, v4, v5, vcc
	v_add_u32_e32 v5, 1, v2
	v_cmp_ge_u32_e32 vcc, v4, v3
	v_add_u32_e32 v4, 1, v6
	s_nop 0
	v_cndmask_b32_e32 v2, v2, v5, vcc
	v_mul_lo_u32 v5, v3, v2
	v_add_u32_e32 v3, v5, v3
	v_cmp_ne_u32_e32 vcc, v4, v3
	s_and_saveexec_b64 s[0:1], vcc
	s_xor_b64 s[10:11], exec, s[0:1]
	s_cbranch_execz .LBB0_461
	s_waitcnt lgkmcnt(0)
	s_add_u32 s16, s52, 0x7500
	s_addc_u32 s17, s53, 0
	v_mov_b32_e32 v1, 0
	global_load_dword v1, v1, s[16:17] sc1
	s_waitcnt vmcnt(0)
	v_cmp_eq_u32_e32 vcc, v1, v2
	s_and_saveexec_b64 s[12:13], vcc
	s_cbranch_execz .LBB0_460
	s_add_u32 s14, s52, 0x4200
	s_addc_u32 s15, s53, 0
	s_mov_b32 s0, 1
	s_mov_b64 s[18:19], 0
	v_mov_b32_e32 v1, 0
	s_branch .LBB0_451

.LBB0_1802:
	s_or_b64 exec, exec, s[14:15]
	v_cvt_f32_u32_e32 v5, v3
	s_waitcnt vmcnt(0)
	v_readfirstlane_b32 s0, v4
	v_sub_u32_e32 v4, 0, v3
	v_rcp_iflag_f32_e32 v5, v5
	v_add_u32_e32 v6, s0, v2
	v_mul_f32_e32 v5, 0x4f7ffffe, v5
	v_cvt_u32_f32_e32 v5, v5
	v_mul_lo_u32 v2, v4, v5
	v_mul_hi_u32 v2, v5, v2
	v_add_u32_e32 v2, v5, v2
	v_mul_hi_u32 v2, v6, v2
	v_mul_lo_u32 v4, v2, v3
	v_sub_u32_e32 v4, v6, v4
	v_add_u32_e32 v5, 1, v2
	v_cmp_ge_u32_e32 vcc, v4, v3
	s_nop 1
	v_cndmask_b32_e32 v2, v2, v5, vcc
	v_sub_u32_e32 v5, v4, v3
	v_cndmask_b32_e32 v4, v4, v5, vcc
	v_add_u32_e32 v5, 1, v2
	v_cmp_ge_u32_e32 vcc, v4, v3
	v_add_u32_e32 v4, 1, v6
	s_nop 0
	v_cndmask_b32_e32 v2, v2, v5, vcc
	v_mul_lo_u32 v5, v3, v2
	v_add_u32_e32 v3, v5, v3
	v_cmp_ne_u32_e32 vcc, v4, v3
	s_and_saveexec_b64 s[0:1], vcc
	s_xor_b64 s[12:13], exec, s[0:1]
	s_cbranch_execz .LBB0_1816
	s_waitcnt lgkmcnt(0)
	s_add_u32 s18, s52, 0x7500
	s_addc_u32 s19, s53, 0
	v_mov_b32_e32 v1, 0
	global_load_dword v1, v1, s[18:19] sc1
	s_waitcnt vmcnt(0)
	v_cmp_eq_u32_e32 vcc, v1, v2
	s_and_saveexec_b64 s[14:15], vcc
	s_cbranch_execz .LBB0_1815
	s_add_u32 s16, s52, 0x4200
	s_addc_u32 s17, s53, 0
	s_mov_b32 s0, 1
	s_mov_b64 s[20:21], 0
	v_mov_b32_e32 v1, 0
	s_branch .LBB0_1806

.LBB0_1959:
	s_or_b64 exec, exec, s[14:15]
	v_cvt_f32_u32_e32 v5, v3
	s_waitcnt vmcnt(0)
	v_readfirstlane_b32 s0, v4
	v_sub_u32_e32 v4, 0, v3
	v_rcp_iflag_f32_e32 v5, v5
	v_add_u32_e32 v6, s0, v2
	v_mul_f32_e32 v5, 0x4f7ffffe, v5
	v_cvt_u32_f32_e32 v5, v5
	v_mul_lo_u32 v2, v4, v5
	v_mul_hi_u32 v2, v5, v2
	v_add_u32_e32 v2, v5, v2
	v_mul_hi_u32 v2, v6, v2
	v_mul_lo_u32 v4, v2, v3
	v_sub_u32_e32 v4, v6, v4
	v_add_u32_e32 v5, 1, v2
	v_cmp_ge_u32_e32 vcc, v4, v3
	s_nop 1
	v_cndmask_b32_e32 v2, v2, v5, vcc
	v_sub_u32_e32 v5, v4, v3
	v_cndmask_b32_e32 v4, v4, v5, vcc
	v_add_u32_e32 v5, 1, v2
	v_cmp_ge_u32_e32 vcc, v4, v3
	v_add_u32_e32 v4, 1, v6
	s_nop 0
	v_cndmask_b32_e32 v2, v2, v5, vcc
	v_mul_lo_u32 v5, v3, v2
	v_add_u32_e32 v3, v5, v3
	v_cmp_ne_u32_e32 vcc, v4, v3
	s_and_saveexec_b64 s[0:1], vcc
	s_xor_b64 s[12:13], exec, s[0:1]
	s_cbranch_execz .LBB0_1973
	s_waitcnt lgkmcnt(0)
	v_readlane_b32 s18, v254, 25
	v_readlane_b32 s19, v254, 26
	s_nop 3
	s_add_u32 s18, s18, 0x7500
	s_addc_u32 s19, s19, 0
	v_mov_b32_e32 v1, 0
	global_load_dword v1, v1, s[18:19] sc1
	s_waitcnt vmcnt(0)
	v_cmp_eq_u32_e32 vcc, v1, v2
	s_and_saveexec_b64 s[14:15], vcc
	s_cbranch_execz .LBB0_1972
	v_readlane_b32 s0, v254, 25
	v_readlane_b32 s1, v254, 26
	s_add_u32 s16, s0, 0x4200
	s_addc_u32 s17, s1, 0
	s_mov_b32 s0, 1
	s_mov_b64 s[20:21], 0
	v_mov_b32_e32 v1, 0
	s_branch .LBB0_1963

.LBB0_3604:
	s_or_b64 exec, exec, s[10:11]
	v_cvt_f32_u32_e32 v5, v3
	s_waitcnt vmcnt(0)
	v_readfirstlane_b32 s0, v4
	v_sub_u32_e32 v4, 0, v3
	v_rcp_iflag_f32_e32 v5, v5
	v_add_u32_e32 v6, s0, v2
	v_mul_f32_e32 v5, 0x4f7ffffe, v5
	v_cvt_u32_f32_e32 v5, v5
	v_mul_lo_u32 v2, v4, v5
	v_mul_hi_u32 v2, v5, v2
	v_add_u32_e32 v2, v5, v2
	v_mul_hi_u32 v2, v6, v2
	v_mul_lo_u32 v4, v2, v3
	v_sub_u32_e32 v4, v6, v4
	v_add_u32_e32 v5, 1, v2
	v_cmp_ge_u32_e32 vcc, v4, v3
	s_nop 1
	v_cndmask_b32_e32 v2, v2, v5, vcc
	v_sub_u32_e32 v5, v4, v3
	v_cndmask_b32_e32 v4, v4, v5, vcc
	v_add_u32_e32 v5, 1, v2
	v_cmp_ge_u32_e32 vcc, v4, v3
	v_add_u32_e32 v4, 1, v6
	s_nop 0
	v_cndmask_b32_e32 v2, v2, v5, vcc
	v_mul_lo_u32 v5, v3, v2
	v_add_u32_e32 v3, v5, v3
	v_cmp_ne_u32_e32 vcc, v4, v3
	s_and_saveexec_b64 s[0:1], vcc
	s_xor_b64 s[8:9], exec, s[0:1]
	s_cbranch_execz .LBB0_3618
	s_waitcnt lgkmcnt(0)
	s_add_u32 s14, s52, 0x7500
	s_addc_u32 s15, s53, 0
	v_mov_b32_e32 v1, 0
	global_load_dword v1, v1, s[14:15] sc1
	s_waitcnt vmcnt(0)
	v_cmp_eq_u32_e32 vcc, v1, v2
	s_and_saveexec_b64 s[10:11], vcc
	s_cbranch_execz .LBB0_3617
	s_add_u32 s12, s52, 0x4200
	s_addc_u32 s13, s53, 0
	s_mov_b32 s0, 1
	s_mov_b64 s[16:17], 0
	v_mov_b32_e32 v1, 0
	s_branch .LBB0_3608
